# cache policy: nt additionally on w_in output stores, final output stores and prep's once-read input row loads
# baseline (speedup 1.0000x reference)
; __device__ __forceinline__ unsigned cvt_pk_bf16(float lo, float hi) { unsigned r; asm volatile("v_cvt_pk_bf16_f32 %0, %1, %2" : "=v"(r) : "v"(lo), "v"(hi)); return r; }
;     __device__ __forceinline__ void operator()(const f32x4 (&acc)[2][2][4][2], const Unit& u, int wr, int wc, int fr, int fq) const {
;         const int row0 = u.pm * BM + wr * 64 + fr, col0 = u.pn * BM + wc * 64 + 8 * fq;
; #pragma unroll
;         for (int ai = 0; ai < 2; ++ai)
; #pragma unroll
;             for (int m = 0; m < 4; ++m) { bf16_t* rowp = O + (size_t)(row0 + ai * HALF + m * 16) * NU + col0;
; #pragma unroll
;                 for (int bj = 0; bj < 2; ++bj) { const f32x4 v0 = acc[ai][bj][m][0] * scale, v1 = acc[ai][bj][m][1] * scale;
;                     u32x4 w; w.x = cvt_pk_bf16(v0[0], v0[1]); w.y = cvt_pk_bf16(v0[2], v0[3]); w.z = cvt_pk_bf16(v1[0], v1[1]); w.w = cvt_pk_bf16(v1[2], v1[3]);
;                     *(u32x4*)(rowp + bj * 32) = w; } }
;     }
.LBB0_271:
	v_lshl_or_b32 v4, s52, 8, v184
	v_lshl_add_u32 v16, s54, 8, v181
	v_ashrrev_i32_e32 v5, 31, v4
	v_mov_b64_e32 v[2:3], s[38:39]
	v_mad_i64_i32 v[6:7], s[34:35], v16, s30, v[2:3]
	v_lshlrev_b64 v[4:5], 1, v[4:5]
	v_lshl_add_u64 v[10:11], v[6:7], 0, v[4:5]
	v_pk_mul_f32 v[6:7], v[158:159], s[20:21] op_sel_hi:[1,0]
	s_nop 15
	s_nop 15
	v_pk_mul_f32 v[8:9], v[160:161], s[20:21] op_sel_hi:[1,0]
	v_cvt_pk_bf16_f32 v6, v6, v7
	v_pk_mul_f32 v[12:13], v[156:157], s[20:21] op_sel_hi:[1,0]
	v_cvt_pk_bf16_f32 v7, v8, v9
	v_pk_mul_f32 v[14:15], v[154:155], s[20:21] op_sel_hi:[1,0]
	s_andn2_b64 vcc, exec, s[42:43]
	v_cvt_pk_bf16_f32 v8, v14, v15
	v_cvt_pk_bf16_f32 v9, v12, v13
	global_store_dwordx4 v[10:11], v[6:9], off nt
	v_pk_mul_f32 v[12:13], v[144:145], s[20:21] op_sel_hi:[1,0]
	v_pk_mul_f32 v[14:15], v[142:143], s[20:21] op_sel_hi:[1,0]
	v_pk_mul_f32 v[6:7], v[150:151], s[20:21] op_sel_hi:[1,0]
	v_pk_mul_f32 v[8:9], v[152:153], s[20:21] op_sel_hi:[1,0]
	v_cvt_pk_bf16_f32 v6, v6, v7
	v_readlane_b32 s90, v254, 28
	v_cvt_pk_bf16_f32 v7, v8, v9
	v_cvt_pk_bf16_f32 v8, v14, v15
	v_cvt_pk_bf16_f32 v9, v12, v13
	global_store_dwordx4 v[10:11], v[6:9], off offset:64 nt
	v_pk_mul_f32 v[12:13], v[140:141], s[20:21] op_sel_hi:[1,0]
	v_pk_mul_f32 v[14:15], v[138:139], s[20:21] op_sel_hi:[1,0]
	v_or_b32_e32 v6, 16, v16
	v_mad_i64_i32 v[6:7], s[34:35], v6, s30, v[2:3]
	v_lshl_add_u64 v[10:11], v[6:7], 0, v[4:5]
	v_pk_mul_f32 v[6:7], v[146:147], s[20:21] op_sel_hi:[1,0]
	v_pk_mul_f32 v[8:9], v[148:149], s[20:21] op_sel_hi:[1,0]
	v_cvt_pk_bf16_f32 v6, v6, v7
	v_readlane_b32 s89, v254, 30
	v_cvt_pk_bf16_f32 v7, v8, v9
	v_cvt_pk_bf16_f32 v8, v14, v15
	v_cvt_pk_bf16_f32 v9, v12, v13
	global_store_dwordx4 v[10:11], v[6:9], off nt
	v_pk_mul_f32 v[12:13], v[128:129], s[20:21] op_sel_hi:[1,0]
	v_pk_mul_f32 v[14:15], v[126:127], s[20:21] op_sel_hi:[1,0]
	v_pk_mul_f32 v[6:7], v[134:135], s[20:21] op_sel_hi:[1,0]
	v_pk_mul_f32 v[8:9], v[136:137], s[20:21] op_sel_hi:[1,0]
	v_cvt_pk_bf16_f32 v6, v6, v7
	v_readlane_b32 s91, v254, 29
	v_cvt_pk_bf16_f32 v7, v8, v9
	v_cvt_pk_bf16_f32 v8, v14, v15
	v_cvt_pk_bf16_f32 v9, v12, v13
	global_store_dwordx4 v[10:11], v[6:9], off offset:64 nt
	v_pk_mul_f32 v[12:13], v[124:125], s[20:21] op_sel_hi:[1,0]
	v_pk_mul_f32 v[14:15], v[122:123], s[20:21] op_sel_hi:[1,0]
	v_or_b32_e32 v6, 32, v16
	v_mad_i64_i32 v[6:7], s[34:35], v6, s30, v[2:3]
	v_lshl_add_u64 v[10:11], v[6:7], 0, v[4:5]
	v_pk_mul_f32 v[6:7], v[130:131], s[20:21] op_sel_hi:[1,0]
	v_pk_mul_f32 v[8:9], v[132:133], s[20:21] op_sel_hi:[1,0]
	v_cvt_pk_bf16_f32 v6, v6, v7
	s_nop 0
	v_cvt_pk_bf16_f32 v7, v8, v9
	v_cvt_pk_bf16_f32 v8, v14, v15
	v_cvt_pk_bf16_f32 v9, v12, v13
	global_store_dwordx4 v[10:11], v[6:9], off nt
	v_pk_mul_f32 v[12:13], v[112:113], s[20:21] op_sel_hi:[1,0]
	v_pk_mul_f32 v[14:15], v[110:111], s[20:21] op_sel_hi:[1,0]
	v_pk_mul_f32 v[6:7], v[118:119], s[20:21] op_sel_hi:[1,0]
	v_pk_mul_f32 v[8:9], v[120:121], s[20:21] op_sel_hi:[1,0]
	v_cvt_pk_bf16_f32 v6, v6, v7
	s_nop 0
	v_cvt_pk_bf16_f32 v7, v8, v9
	v_cvt_pk_bf16_f32 v8, v14, v15
	v_cvt_pk_bf16_f32 v9, v12, v13
	global_store_dwordx4 v[10:11], v[6:9], off offset:64 nt
	v_pk_mul_f32 v[12:13], v[108:109], s[20:21] op_sel_hi:[1,0]
	v_pk_mul_f32 v[14:15], v[106:107], s[20:21] op_sel_hi:[1,0]
	v_or_b32_e32 v6, 48, v16
	v_mad_i64_i32 v[6:7], s[34:35], v6, s30, v[2:3]
	v_lshl_add_u64 v[10:11], v[6:7], 0, v[4:5]
	v_pk_mul_f32 v[6:7], v[114:115], s[20:21] op_sel_hi:[1,0]
	v_pk_mul_f32 v[8:9], v[116:117], s[20:21] op_sel_hi:[1,0]
	v_cvt_pk_bf16_f32 v6, v6, v7
	s_nop 0
	v_cvt_pk_bf16_f32 v7, v8, v9
	v_cvt_pk_bf16_f32 v8, v14, v15
	v_cvt_pk_bf16_f32 v9, v12, v13
	global_store_dwordx4 v[10:11], v[6:9], off nt
	v_pk_mul_f32 v[12:13], v[100:101], s[20:21] op_sel_hi:[1,0]
	v_pk_mul_f32 v[14:15], v[98:99], s[20:21] op_sel_hi:[1,0]
	v_pk_mul_f32 v[6:7], v[102:103], s[20:21] op_sel_hi:[1,0]
	v_pk_mul_f32 v[8:9], v[104:105], s[20:21] op_sel_hi:[1,0]
	v_cvt_pk_bf16_f32 v6, v6, v7
	s_nop 0
	v_cvt_pk_bf16_f32 v7, v8, v9
	v_cvt_pk_bf16_f32 v8, v14, v15
; __device__ __forceinline__ unsigned cvt_pk_bf16(float lo, float hi) { unsigned r; asm volatile("v_cvt_pk_bf16_f32 %0, %1, %2" : "=v"(r) : "v"(lo), "v"(hi)); return r; }
; #define PG8_BAR __builtin_amdgcn_s_barrier()
; template <class Epi, class Sched, bool GATHER, bool F8 = false>
; __device__ __forceinline__ void gemm_phase(LAS unsigned char* lds, const Gemm g, const Sched& S, const Epi& E, const int tid) {
;     ...
;         cur = nxt; cB = nB; cA = nA; ++ui;
;         if constexpr (GATHER) {
; #pragma unroll
;             for (int h = 0; h < 2; ++h)
; #pragma unroll
;                 for (int i = 0; i < 2; ++i) oc[h][i] = on[h][i]; }
;         if (wr == 1) PG8_BAR;
;     __device__ __forceinline__ void operator()(const f32x4 (&acc)[2][2][4][2], const Unit& u, int wr, int wc, int fr, int fq) const {
;         const int row0 = u.pm * BM + wr * 64 + fr, col0 = u.pn * BM + wc * 64 + 8 * fq;
; #pragma unroll
;         for (int ai = 0; ai < 2; ++ai)
; #pragma unroll
;             for (int m = 0; m < 4; ++m) { bf16_t* rowp = O + (size_t)(row0 + ai * HALF + m * 16) * NU + col0;
; #pragma unroll
;                 for (int bj = 0; bj < 2; ++bj) { const f32x4 v0 = acc[ai][bj][m][0] * scale, v1 = acc[ai][bj][m][1] * scale;
;                     u32x4 w; w.x = cvt_pk_bf16(v0[0], v0[1]); w.y = cvt_pk_bf16(v0[2], v0[3]); w.z = cvt_pk_bf16(v1[0], v1[1]); w.w = cvt_pk_bf16(v1[2], v1[3]);
;                     *(u32x4*)(rowp + bj * 32) = w; } }
;     }
	v_cvt_pk_bf16_f32 v9, v12, v13
	global_store_dwordx4 v[10:11], v[6:9], off offset:64 nt
	v_pk_mul_f32 v[12:13], v[92:93], s[20:21] op_sel_hi:[1,0]
	v_pk_mul_f32 v[14:15], v[90:91], s[20:21] op_sel_hi:[1,0]
	v_add_u32_e32 v6, 0x80, v16
	v_mad_i64_i32 v[6:7], s[34:35], v6, s30, v[2:3]
	v_lshl_add_u64 v[10:11], v[6:7], 0, v[4:5]
	v_pk_mul_f32 v[6:7], v[94:95], s[20:21] op_sel_hi:[1,0]
	v_pk_mul_f32 v[8:9], v[96:97], s[20:21] op_sel_hi:[1,0]
	v_cvt_pk_bf16_f32 v6, v6, v7
	s_nop 0
	v_cvt_pk_bf16_f32 v7, v8, v9
	v_cvt_pk_bf16_f32 v8, v14, v15
	v_cvt_pk_bf16_f32 v9, v12, v13
	global_store_dwordx4 v[10:11], v[6:9], off nt
	v_pk_mul_f32 v[12:13], v[80:81], s[20:21] op_sel_hi:[1,0]
	v_pk_mul_f32 v[14:15], v[78:79], s[20:21] op_sel_hi:[1,0]
	v_pk_mul_f32 v[6:7], v[86:87], s[20:21] op_sel_hi:[1,0]
	v_pk_mul_f32 v[8:9], v[88:89], s[20:21] op_sel_hi:[1,0]
	v_cvt_pk_bf16_f32 v6, v6, v7
	s_nop 0
	v_cvt_pk_bf16_f32 v7, v8, v9
	v_cvt_pk_bf16_f32 v8, v14, v15
	v_cvt_pk_bf16_f32 v9, v12, v13
	global_store_dwordx4 v[10:11], v[6:9], off offset:64 nt
	v_pk_mul_f32 v[12:13], v[76:77], s[20:21] op_sel_hi:[1,0]
	v_pk_mul_f32 v[14:15], v[74:75], s[20:21] op_sel_hi:[1,0]
	v_add_u32_e32 v6, 0x90, v16
	v_mad_i64_i32 v[6:7], s[34:35], v6, s30, v[2:3]
	v_lshl_add_u64 v[10:11], v[6:7], 0, v[4:5]
	v_pk_mul_f32 v[6:7], v[82:83], s[20:21] op_sel_hi:[1,0]
	v_pk_mul_f32 v[8:9], v[84:85], s[20:21] op_sel_hi:[1,0]
	v_cvt_pk_bf16_f32 v6, v6, v7
	s_nop 0
	v_cvt_pk_bf16_f32 v7, v8, v9
	v_cvt_pk_bf16_f32 v8, v14, v15
	v_cvt_pk_bf16_f32 v9, v12, v13
	global_store_dwordx4 v[10:11], v[6:9], off nt
	v_pk_mul_f32 v[12:13], v[64:65], s[20:21] op_sel_hi:[1,0]
	v_pk_mul_f32 v[14:15], v[62:63], s[20:21] op_sel_hi:[1,0]
	v_pk_mul_f32 v[6:7], v[70:71], s[20:21] op_sel_hi:[1,0]
	v_pk_mul_f32 v[8:9], v[72:73], s[20:21] op_sel_hi:[1,0]
	v_cvt_pk_bf16_f32 v6, v6, v7
	s_nop 0
	v_cvt_pk_bf16_f32 v7, v8, v9
	v_cvt_pk_bf16_f32 v8, v14, v15
	v_cvt_pk_bf16_f32 v9, v12, v13
	global_store_dwordx4 v[10:11], v[6:9], off offset:64 nt
	v_pk_mul_f32 v[12:13], v[60:61], s[20:21] op_sel_hi:[1,0]
	v_pk_mul_f32 v[14:15], v[58:59], s[20:21] op_sel_hi:[1,0]
	v_add_u32_e32 v6, 0xa0, v16
	v_mad_i64_i32 v[6:7], s[34:35], v6, s30, v[2:3]
	v_lshl_add_u64 v[10:11], v[6:7], 0, v[4:5]
	v_pk_mul_f32 v[6:7], v[66:67], s[20:21] op_sel_hi:[1,0]
	v_pk_mul_f32 v[8:9], v[68:69], s[20:21] op_sel_hi:[1,0]
	v_cvt_pk_bf16_f32 v6, v6, v7
	s_nop 0
	v_cvt_pk_bf16_f32 v7, v8, v9
	v_cvt_pk_bf16_f32 v8, v14, v15
	v_cvt_pk_bf16_f32 v9, v12, v13
	global_store_dwordx4 v[10:11], v[6:9], off nt
	v_pk_mul_f32 v[12:13], v[48:49], s[20:21] op_sel_hi:[1,0]
	v_pk_mul_f32 v[14:15], v[46:47], s[20:21] op_sel_hi:[1,0]
	v_pk_mul_f32 v[6:7], v[54:55], s[20:21] op_sel_hi:[1,0]
	v_pk_mul_f32 v[8:9], v[56:57], s[20:21] op_sel_hi:[1,0]
	v_cvt_pk_bf16_f32 v6, v6, v7
	s_nop 0
	v_cvt_pk_bf16_f32 v7, v8, v9
	v_cvt_pk_bf16_f32 v8, v14, v15
	v_cvt_pk_bf16_f32 v9, v12, v13
	global_store_dwordx4 v[10:11], v[6:9], off offset:64 nt
	v_pk_mul_f32 v[10:11], v[42:43], s[20:21] op_sel_hi:[1,0]
	s_nop 0
	v_add_u32_e32 v6, 0xb0, v16
	v_mad_i64_i32 v[2:3], s[34:35], v6, s30, v[2:3]
	v_lshl_add_u64 v[6:7], v[2:3], 0, v[4:5]
	v_pk_mul_f32 v[4:5], v[52:53], s[20:21] op_sel_hi:[1,0]
	v_pk_mul_f32 v[2:3], v[50:51], s[20:21] op_sel_hi:[1,0]
	v_pk_mul_f32 v[8:9], v[44:45], s[20:21] op_sel_hi:[1,0]
	v_cvt_pk_bf16_f32 v2, v2, v3
	v_cvt_pk_bf16_f32 v3, v4, v5
	v_cvt_pk_bf16_f32 v4, v10, v11
	s_mov_b64 s[34:35], -1
	v_cvt_pk_bf16_f32 v5, v8, v9
	global_store_dwordx4 v[6:7], v[2:5], off nt
	v_pk_mul_f32 v[8:9], v[36:37], s[20:21] op_sel_hi:[1,0]
	v_pk_mul_f32 v[10:11], v[34:35], s[20:21] op_sel_hi:[1,0]
	v_pk_mul_f32 v[4:5], v[40:41], s[20:21] op_sel_hi:[1,0]
	v_pk_mul_f32 v[2:3], v[38:39], s[20:21] op_sel_hi:[1,0]
	s_nop 0
	v_cvt_pk_bf16_f32 v2, v2, v3
	v_cvt_pk_bf16_f32 v3, v4, v5
	v_cvt_pk_bf16_f32 v4, v10, v11
	v_cvt_pk_bf16_f32 v5, v8, v9
	global_store_dwordx4 v[6:7], v[2:5], off offset:64 nt
	s_cbranch_vccnz .LBB0_261
	s_andn2_b64 vcc, exec, s[26:27]
	s_cbranch_vccnz .LBB0_260
	s_barrier
	s_branch .LBB0_260

; __device__ __forceinline__ void qk_rope(const unsigned char* ws, int row, int j, float (&cs)[8], float (&sn)[8]) {
;     if (row < TL) { const float* rp = (const float*)(ws + WS_ROPE) + (size_t)(row & (SEQ - 1)) * 64 + 32 * (j >> 2) + 8 * (j & 1);
;         const f32x4 c0 = *(const f32x4*)rp, c1 = *(const f32x4*)(rp + 4), s0 = *(const f32x4*)(rp + 16), s1 = *(const f32x4*)(rp + 20); const float sg = (j & 2) ? 1.f : -1.f;
; #pragma unroll
;         for (int e = 0; e < 4; ++e) { cs[e] = c0[e]; cs[4 + e] = c1[e]; sn[e] = sg * s0[e]; sn[4 + e] = sg * s1[e]; } }
; __device__ __forceinline__ void prep_qk_rows4(KP Pk, Frame& F, int l, int row0) {
;     unsigned char* ws = F.ws;
;     bf16_t* U = (bf16_t*)(ws + WS_U);
;     const int j = F.lane & 7; const float qs = 0.125f * LOG2E;
;     u32x4 raw[4][3], rawk;
; #pragma unroll
;     for (int r = 0; r < 4; ++r) { const bf16_t* up = U + (size_t)(row0 + r) * NU + 8 * F.lane; raw[r][0] = *(const u32x4*)(up + UC_SQ); raw[r][1] = *(const u32x4*)(up + UC_DQ); raw[r][2] = *(const u32x4*)(up + UC_DK); }
;     const int rowk = row0 + (F.lane >> 4);
;     rawk = *(const u32x4*)(U + (size_t)rowk * NU + UC_SK + 8 * (F.lane & 15));
;     float wsq[8], wdq[8], wdk[8], wsk[8];
;     { const float* a = Pk->in[I_SQN] + l * 64 + 8 * j; const float* b = Pk->in[I_DQN] + l * 64 + 8 * j; const float* c = Pk->in[I_DKN] + l * 64 + 8 * j; const float* d = Pk->in[I_SKN] + l * 64 + 8 * j;
; #pragma unroll
;       for (int e = 0; e < 8; ++e) { wsq[e] = a[e] * qs; wdq[e] = b[e] * qs; wdk[e] = c[e]; wsk[e] = d[e]; } }
;     float cs[4][8], sn[4][8], csk[8], snk[8];
; #pragma unroll
;     for (int r = 0; r < 4; ++r) qk_rope(ws, row0 + r, j, cs[r], sn[r]);
;     qk_rope(ws, rowk, j, csk, snk);
.LBB0_366:
	s_cmp_ge_i32 s48, s6
	s_mov_b64 s[8:9], -1
	s_cbranch_scc0 .LBB0_402
	s_sub_i32 s4, s48, s6
	s_cmpk_gt_i32 s4, 0x47f
	s_cbranch_scc0 .LBB0_394
	s_cmpk_gt_u32 s4, 0x6bf
	s_cbranch_scc0 .LBB0_386
	s_lshl_b32 s5, s4, 2
	s_add_i32 s18, s5, 0xffffe500
	s_mul_i32 s60, s18, 0x1500
	v_lshl_add_u64 v[198:199], s[60:61], 1, v[118:119]
	v_add_co_u32_e32 v2, vcc, 0x1000, v198
	s_add_i32 s8, s60, 0x1500
	s_nop 0
	v_addc_co_u32_e32 v3, vcc, 0, v199, vcc
	s_mov_b32 s9, s61
	global_load_dwordx4 v[94:97], v[2:3], off offset:3584 nt
	v_add_co_u32_e32 v2, vcc, 0x2000, v198
	v_lshl_add_u64 v[162:163], s[8:9], 1, v[118:119]
	s_add_i32 s8, s60, 0x2a00
	v_addc_co_u32_e32 v3, vcc, 0, v199, vcc
	v_lshl_add_u64 v[134:135], s[8:9], 1, v[118:119]
	global_load_dwordx4 v[90:93], v[2:3], off offset:512 nt
	global_load_dwordx4 v[58:61], v[134:135], off offset:3072 nt
	v_add_co_u32_e32 v2, vcc, 0x1000, v162
	global_load_dwordx4 v[86:89], v[162:163], off offset:3072 nt
	s_nop 0
	v_addc_co_u32_e32 v3, vcc, 0, v163, vcc
	global_load_dwordx4 v[74:77], v[2:3], off offset:3584 nt
	v_add_co_u32_e32 v2, vcc, 0x2000, v162
	s_addk_i32 s60, 0x3f00
	s_nop 0
	v_addc_co_u32_e32 v3, vcc, 0, v163, vcc
	global_load_dwordx4 v[62:65], v[2:3], off offset:512 nt
	v_add_co_u32_e32 v2, vcc, 0x1000, v134
	v_lshl_add_u64 v[132:133], s[60:61], 1, v[118:119]
	s_nop 0
	v_addc_co_u32_e32 v3, vcc, 0, v135, vcc
	global_load_dwordx4 v[54:57], v[2:3], off offset:3584 nt
	v_add_co_u32_e32 v2, vcc, 0x2000, v134
	global_load_dwordx4 v[98:101], v[198:199], off offset:3072 nt
	s_nop 0
	v_addc_co_u32_e32 v3, vcc, 0, v135, vcc
	global_load_dwordx4 v[50:53], v[2:3], off offset:512 nt
	v_add_co_u32_e32 v2, vcc, 0x1000, v132
	s_load_dwordx4 s[52:55], s[16:17], 0x68
	s_load_dwordx4 s[56:59], s[16:17], 0xc8
	v_addc_co_u32_e32 v3, vcc, 0, v133, vcc
	global_load_dwordx4 v[42:45], v[2:3], off offset:3584 nt
	v_add_co_u32_e32 v2, vcc, 0x2000, v132
	v_add_u32_e32 v16, s18, v1
	s_nop 0
	v_addc_co_u32_e32 v3, vcc, 0, v133, vcc
	global_load_dwordx4 v[38:41], v[2:3], off offset:512 nt
	v_mov_b64_e32 v[2:3], s[42:43]
	v_mad_i64_i32 v[2:3], s[8:9], v16, s30, v[2:3]
	s_waitcnt lgkmcnt(0)
	s_add_u32 s8, s52, s44
	s_addc_u32 s9, s53, s45
	s_add_u32 s26, s56, s44
	v_lshlrev_b32_e32 v4, 1, v120
	v_mov_b32_e32 v5, v0
	s_addc_u32 s27, s57, s45
	v_lshl_add_u64 v[160:161], v[2:3], 0, v[4:5]
	s_add_u32 s34, s58, s44
	v_add_co_u32_e32 v2, vcc, s1, v160
	s_addc_u32 s35, s59, s45
	s_nop 0
	v_addc_co_u32_e32 v3, vcc, 0, v161, vcc
	s_add_u32 s50, s54, s44
	global_load_dwordx4 v[46:49], v[132:133], off offset:3072 nt
	global_load_dwordx4 v[30:33], v[2:3], off nt
	s_addc_u32 s51, s55, s45
	global_load_dwordx4 v[110:113], v249, s[8:9] offset:16
	global_load_dwordx4 v[102:105], v249, s[8:9]
	global_load_dwordx4 v[114:117], v249, s[26:27] offset:16
	global_load_dwordx4 v[106:109], v249, s[26:27]
	global_load_dwordx4 v[26:29], v249, s[34:35] offset:16
	global_load_dwordx4 v[34:37], v249, s[34:35]
	global_load_dwordx4 v[2:5], v249, s[50:51] offset:16
	global_load_dwordx4 v[22:25], v249, s[50:51]
	s_cmpk_lt_u32 s18, 0x4000
	s_cbranch_scc0 .LBB0_371
	s_lshl_b32 s8, s18, 8
	s_and_b32 s60, s8, 0x7fc00
	v_lshl_add_u64 v[14:15], v[122:123], 0, s[60:61]
	global_load_dwordx4 v[6:9], v[14:15], off
	global_load_dwordx4 v[10:13], v[14:15], off offset:16
	global_load_dwordx4 v[18:21], v[14:15], off offset:80
	global_load_dwordx4 v[66:69], v[14:15], off offset:64
	s_waitcnt vmcnt(0)
	v_mov_b32_e32 v214, v6
	v_mov_b32_e32 v212, v7
	v_mov_b32_e32 v215, v8
	v_mov_b32_e32 v14, v66
	v_mov_b32_e32 v15, v68
	v_pk_mul_f32 v[206:207], v[124:125], v[14:15]
	v_mov_b32_e32 v14, v18
	v_mov_b32_e32 v15, v20
	v_mov_b32_e32 v68, v67
	v_mov_b32_e32 v20, v19
	v_pk_mul_f32 v[200:201], v[124:125], v[14:15]
	v_pk_mul_f32 v[202:203], v[124:125], v[68:69]
	v_pk_mul_f32 v[204:205], v[124:125], v[20:21]
	v_mov_b32_e32 v213, v9
	v_mov_b32_e32 v210, v10
	v_mov_b32_e32 v208, v11
	v_mov_b32_e32 v211, v12
	v_mov_b32_e32 v209, v13
	s_cmpk_lt_u32 s18, 0x3fff
	s_mov_b64 s[8:9], -1
	s_cbranch_scc0 .LBB0_372
	s_branch .LBB0_373

; __device__ __forceinline__ void add_y2(const unsigned char* y0, const unsigned char* y1, const float* gf, int lane, f32x4 (&v)[8]) {
; #pragma unroll
;     for (int j = 0; j < 8; ++j) { const unsigned a = ((const unsigned*)y0)[lane + 64 * j], b = ((const unsigned*)y1)[lane + 64 * j]; const f32x4 g = ((const f32x4*)gf)[lane + 64 * j] * (1.f / 32.f);
;         const f32x2 a0 = __builtin_amdgcn_cvt_pk_f32_fp8(a, false), a1 = __builtin_amdgcn_cvt_pk_f32_fp8(a, true), b0 = __builtin_amdgcn_cvt_pk_f32_fp8(b, false), b1 = __builtin_amdgcn_cvt_pk_f32_fp8(b, true);
;         v[j][0] += g[0] * (a0[0] + b0[0]); v[j][1] += g[1] * (a0[1] + b0[1]); v[j][2] += g[2] * (a1[0] + b1[0]); v[j][3] += g[3] * (a1[1] + b1[1]); }
; __device__ __forceinline__ void ph_final(KP Pk, Frame& F) {
;     ...
;     for (int row = gw; row < TL; row += NGW) { f32x4 v[8];
;         load_row_bf16(X + (size_t)row * D, F.lane, v);
;         add_y2(Y2 + (size_t)row * D, Y2 + ((size_t)TT + row) * D, (const float*)(ws + WS_MOD) + ((size_t)9 + (row >> 11)) * 12288 + 5 * D, F.lane, v);
.LBB0_1445:
	s_ashr_i32 s0, s20, 11
	v_lshl_add_u64 v[10:11], s[6:7], 0, v[4:5]
	s_add_i32 s16, s0, 9
	v_add_co_u32_e64 v12, s[0:1], s13, v10
	v_lshl_add_u64 v[8:9], s[6:7], 0, v[2:3]
	s_nop 0
	v_addc_co_u32_e64 v13, s[0:1], 0, v11, s[0:1]
	v_add_co_u32_e64 v10, s[0:1], s14, v10
	v_add_co_u32_e32 v8, vcc, 0x1d600000, v8
	s_nop 0
	v_addc_co_u32_e64 v11, s[0:1], 0, v11, s[0:1]
	s_mul_hi_i32 s1, s16, 0xc000
	s_mul_i32 s16, s16, 0xc000
	global_load_dword v60, v[12:13], off
	global_load_dword v62, v[10:11], off
	global_load_dword v66, v[12:13], off offset:256
	global_load_dword v70, v[10:11], off offset:256
	global_load_dword v74, v[12:13], off offset:512
	global_load_dword v78, v[10:11], off offset:512
	global_load_dword v82, v[12:13], off offset:768
	global_load_dword v86, v[10:11], off offset:768
	global_load_dword v90, v[12:13], off offset:1024
	global_load_dword v94, v[10:11], off offset:1024
	global_load_dword v98, v[12:13], off offset:1280
	global_load_dword v102, v[10:11], off offset:1280
	global_load_dword v106, v[12:13], off offset:1536
	global_load_dword v110, v[10:11], off offset:1536
	global_load_dword v114, v[12:13], off offset:1792
	global_load_dword v118, v[10:11], off offset:1792
	s_add_u32 s0, s6, s16
	v_addc_co_u32_e32 v9, vcc, 0, v9, vcc
	s_addc_u32 s1, s7, s1
	global_load_dwordx2 v[40:41], v[8:9], off
	global_load_dwordx2 v[42:43], v[8:9], off offset:512
	global_load_dwordx2 v[44:45], v[8:9], off offset:1024
	global_load_dwordx2 v[46:47], v[8:9], off offset:1536
	global_load_dwordx2 v[48:49], v[8:9], off offset:2048
	global_load_dwordx2 v[50:51], v[8:9], off offset:2560
	global_load_dwordx2 v[52:53], v[8:9], off offset:3072
	global_load_dwordx2 v[54:55], v[8:9], off offset:3584
	v_lshl_add_u64 v[8:9], v[0:1], 4, s[0:1]
	v_lshl_add_u64 v[56:57], v[8:9], 0, s[10:11]
	v_add_co_u32_e32 v58, vcc, s15, v8
	s_add_i32 s20, s20, s18
	s_nop 0
	v_addc_co_u32_e32 v59, vcc, 0, v9, vcc
	global_load_dwordx4 v[8:11], v[56:57], off offset:1024
	global_load_dwordx4 v[12:15], v[56:57], off offset:2048
	global_load_dwordx4 v[16:19], v[58:59], off offset:-4096
	global_load_dwordx4 v[20:23], v[56:57], off offset:3072
	global_load_dwordx4 v[24:27], v[58:59], off
	global_load_dwordx4 v[28:31], v[58:59], off offset:1024
	global_load_dwordx4 v[32:35], v[58:59], off offset:2048
	global_load_dwordx4 v[36:39], v[58:59], off offset:3072
	v_lshl_add_u64 v[2:3], v[2:3], 0, s[2:3]
	v_lshl_add_u64 v[4:5], v[4:5], 0, s[8:9]
	s_cmpk_lt_i32 s20, 0x4000
	s_waitcnt vmcnt(31)
	v_cvt_pk_f32_fp8_e32 v[56:57], v60
	v_cvt_pk_f32_fp8_sdwa v[58:59], v60 src0_sel:WORD_1
	s_waitcnt vmcnt(30)
	v_cvt_pk_f32_fp8_e32 v[60:61], v62
	v_cvt_pk_f32_fp8_sdwa v[62:63], v62 src0_sel:WORD_1
	s_waitcnt vmcnt(29)
	v_cvt_pk_f32_fp8_e32 v[64:65], v66
	v_cvt_pk_f32_fp8_sdwa v[66:67], v66 src0_sel:WORD_1
	s_waitcnt vmcnt(28)
	v_cvt_pk_f32_fp8_e32 v[68:69], v70
	v_cvt_pk_f32_fp8_sdwa v[70:71], v70 src0_sel:WORD_1
	s_waitcnt vmcnt(27)
	v_cvt_pk_f32_fp8_e32 v[72:73], v74
	v_cvt_pk_f32_fp8_sdwa v[74:75], v74 src0_sel:WORD_1
	s_waitcnt vmcnt(26)
	v_cvt_pk_f32_fp8_e32 v[76:77], v78
	v_cvt_pk_f32_fp8_sdwa v[78:79], v78 src0_sel:WORD_1
	s_waitcnt vmcnt(25)
	v_cvt_pk_f32_fp8_e32 v[80:81], v82
	v_cvt_pk_f32_fp8_sdwa v[82:83], v82 src0_sel:WORD_1
	s_waitcnt vmcnt(24)
	v_cvt_pk_f32_fp8_e32 v[84:85], v86
	v_cvt_pk_f32_fp8_sdwa v[86:87], v86 src0_sel:WORD_1
	s_waitcnt vmcnt(23)
	v_cvt_pk_f32_fp8_e32 v[88:89], v90
	v_cvt_pk_f32_fp8_sdwa v[90:91], v90 src0_sel:WORD_1
	s_waitcnt vmcnt(22)
	v_cvt_pk_f32_fp8_e32 v[92:93], v94
	v_cvt_pk_f32_fp8_sdwa v[94:95], v94 src0_sel:WORD_1
	s_waitcnt vmcnt(21)
	v_cvt_pk_f32_fp8_e32 v[96:97], v98
	v_cvt_pk_f32_fp8_sdwa v[98:99], v98 src0_sel:WORD_1
	s_waitcnt vmcnt(20)
	v_cvt_pk_f32_fp8_e32 v[100:101], v102
	v_cvt_pk_f32_fp8_sdwa v[102:103], v102 src0_sel:WORD_1
	s_waitcnt vmcnt(19)
	v_cvt_pk_f32_fp8_e32 v[104:105], v106
	v_cvt_pk_f32_fp8_sdwa v[106:107], v106 src0_sel:WORD_1
	s_waitcnt vmcnt(18)
	v_cvt_pk_f32_fp8_e32 v[108:109], v110
	v_cvt_pk_f32_fp8_sdwa v[110:111], v110 src0_sel:WORD_1
	s_waitcnt vmcnt(17)
	v_cvt_pk_f32_fp8_e32 v[112:113], v114
	v_cvt_pk_f32_fp8_sdwa v[114:115], v114 src0_sel:WORD_1
	s_waitcnt vmcnt(16)
	v_cvt_pk_f32_fp8_e32 v[116:117], v118
	v_cvt_pk_f32_fp8_sdwa v[118:119], v118 src0_sel:WORD_1
	s_waitcnt vmcnt(15)
; __device__ __forceinline__ void add_y2(const unsigned char* y0, const unsigned char* y1, const float* gf, int lane, f32x4 (&v)[8]) {
;     ...
;     for (int j = 0; j < 8; ++j) { const unsigned a = ((const unsigned*)y0)[lane + 64 * j], b = ((const unsigned*)y1)[lane + 64 * j]; const f32x4 g = ((const f32x4*)gf)[lane + 64 * j] * (1.f / 32.f);
;         const f32x2 a0 = __builtin_amdgcn_cvt_pk_f32_fp8(a, false), a1 = __builtin_amdgcn_cvt_pk_f32_fp8(a, true), b0 = __builtin_amdgcn_cvt_pk_f32_fp8(b, false), b1 = __builtin_amdgcn_cvt_pk_f32_fp8(b, true);
;         v[j][0] += g[0] * (a0[0] + b0[0]); v[j][1] += g[1] * (a0[1] + b0[1]); v[j][2] += g[2] * (a1[0] + b1[0]); v[j][3] += g[3] * (a1[1] + b1[1]); }
; __device__ __forceinline__ void ph_final(KP Pk, Frame& F) {
;     ...
; #pragma unroll
;         for (int j = 0; j < 8; ++j) ((f32x4*)(Pk->out + (size_t)row * D))[F.lane + 64 * j] = v[j]; }
	v_lshlrev_b32_e32 v120, 16, v40
	v_and_b32_e32 v121, 0xffff0000, v40
	v_lshlrev_b32_e32 v40, 16, v41
	v_and_b32_e32 v41, 0xffff0000, v41
	v_pk_add_f32 v[56:57], v[56:57], v[60:61]
	v_pk_add_f32 v[58:59], v[58:59], v[62:63]
	s_waitcnt vmcnt(5)
	v_pk_mul_f32 v[18:19], v[18:19], s[12:13] op_sel_hi:[1,0]
	v_pk_mul_f32 v[16:17], v[16:17], s[12:13] op_sel_hi:[1,0]
	v_lshlrev_b32_e32 v122, 16, v42
	v_and_b32_e32 v123, 0xffff0000, v42
	v_lshlrev_b32_e32 v42, 16, v43
	v_and_b32_e32 v43, 0xffff0000, v43
	v_lshlrev_b32_e32 v124, 16, v44
	v_and_b32_e32 v125, 0xffff0000, v44
	v_lshlrev_b32_e32 v44, 16, v45
	v_and_b32_e32 v45, 0xffff0000, v45
	v_lshlrev_b32_e32 v126, 16, v46
	v_and_b32_e32 v127, 0xffff0000, v46
	v_lshlrev_b32_e32 v46, 16, v47
	v_and_b32_e32 v47, 0xffff0000, v47
	v_lshlrev_b32_e32 v128, 16, v48
	v_and_b32_e32 v129, 0xffff0000, v48
	v_lshlrev_b32_e32 v48, 16, v49
	v_and_b32_e32 v49, 0xffff0000, v49
	v_lshlrev_b32_e32 v130, 16, v50
	v_and_b32_e32 v131, 0xffff0000, v50
	v_lshlrev_b32_e32 v50, 16, v51
	v_and_b32_e32 v51, 0xffff0000, v51
	v_lshlrev_b32_e32 v132, 16, v52
	v_and_b32_e32 v133, 0xffff0000, v52
	v_lshlrev_b32_e32 v52, 16, v53
	v_and_b32_e32 v53, 0xffff0000, v53
	v_lshlrev_b32_e32 v134, 16, v54
	v_and_b32_e32 v135, 0xffff0000, v54
	v_lshlrev_b32_e32 v54, 16, v55
	v_and_b32_e32 v55, 0xffff0000, v55
	v_pk_add_f32 v[60:61], v[64:65], v[68:69]
	v_pk_add_f32 v[62:63], v[66:67], v[70:71]
	v_pk_add_f32 v[64:65], v[72:73], v[76:77]
	v_pk_add_f32 v[66:67], v[74:75], v[78:79]
	v_pk_add_f32 v[68:69], v[80:81], v[84:85]
	v_pk_add_f32 v[70:71], v[82:83], v[86:87]
	v_pk_add_f32 v[72:73], v[88:89], v[92:93]
	v_pk_add_f32 v[74:75], v[90:91], v[94:95]
	v_pk_add_f32 v[76:77], v[96:97], v[100:101]
	v_pk_add_f32 v[78:79], v[98:99], v[102:103]
	v_pk_add_f32 v[80:81], v[104:105], v[108:109]
	v_pk_add_f32 v[82:83], v[106:107], v[110:111]
	v_pk_add_f32 v[84:85], v[112:113], v[116:117]
	v_pk_add_f32 v[86:87], v[114:115], v[118:119]
	v_pk_mul_f32 v[88:89], v[10:11], s[12:13] op_sel_hi:[1,0]
	v_pk_mul_f32 v[90:91], v[8:9], s[12:13] op_sel_hi:[1,0]
	v_pk_mul_f32 v[92:93], v[14:15], s[12:13] op_sel_hi:[1,0]
	v_pk_mul_f32 v[94:95], v[12:13], s[12:13] op_sel_hi:[1,0]
	s_waitcnt vmcnt(4)
	v_pk_mul_f32 v[22:23], v[22:23], s[12:13] op_sel_hi:[1,0]
	v_pk_mul_f32 v[20:21], v[20:21], s[12:13] op_sel_hi:[1,0]
	s_waitcnt vmcnt(3)
	v_pk_mul_f32 v[26:27], v[26:27], s[12:13] op_sel_hi:[1,0]
	v_pk_mul_f32 v[24:25], v[24:25], s[12:13] op_sel_hi:[1,0]
	s_waitcnt vmcnt(2)
	v_pk_mul_f32 v[30:31], v[30:31], s[12:13] op_sel_hi:[1,0]
	v_pk_mul_f32 v[28:29], v[28:29], s[12:13] op_sel_hi:[1,0]
	s_waitcnt vmcnt(1)
	v_pk_mul_f32 v[34:35], v[34:35], s[12:13] op_sel_hi:[1,0]
	v_pk_mul_f32 v[32:33], v[32:33], s[12:13] op_sel_hi:[1,0]
	s_waitcnt vmcnt(0)
	v_pk_mul_f32 v[38:39], v[38:39], s[12:13] op_sel_hi:[1,0]
	v_pk_mul_f32 v[36:37], v[36:37], s[12:13] op_sel_hi:[1,0]
	v_pk_fma_f32 v[8:9], v[16:17], v[56:57], v[120:121]
	v_pk_fma_f32 v[10:11], v[18:19], v[58:59], v[40:41]
	v_pk_fma_f32 v[12:13], v[90:91], v[60:61], v[122:123]
	v_pk_fma_f32 v[14:15], v[88:89], v[62:63], v[42:43]
	v_pk_fma_f32 v[16:17], v[94:95], v[64:65], v[124:125]
	v_pk_fma_f32 v[18:19], v[92:93], v[66:67], v[44:45]
	v_pk_fma_f32 v[20:21], v[20:21], v[68:69], v[126:127]
	v_pk_fma_f32 v[22:23], v[22:23], v[70:71], v[46:47]
	v_pk_fma_f32 v[24:25], v[24:25], v[72:73], v[128:129]
	v_pk_fma_f32 v[26:27], v[26:27], v[74:75], v[48:49]
	v_pk_fma_f32 v[28:29], v[28:29], v[76:77], v[130:131]
	v_pk_fma_f32 v[30:31], v[30:31], v[78:79], v[50:51]
	v_pk_fma_f32 v[32:33], v[32:33], v[80:81], v[132:133]
	v_pk_fma_f32 v[34:35], v[34:35], v[82:83], v[52:53]
	v_pk_fma_f32 v[36:37], v[36:37], v[84:85], v[134:135]
	v_pk_fma_f32 v[38:39], v[38:39], v[86:87], v[54:55]
	global_store_dwordx4 v[6:7], v[8:11], off offset:-4096 nt
	global_store_dwordx4 v[6:7], v[12:15], off offset:-3072 nt
	global_store_dwordx4 v[6:7], v[16:19], off offset:-2048 nt
	global_store_dwordx4 v[6:7], v[20:23], off offset:-1024 nt
	global_store_dwordx4 v[6:7], v[24:27], off nt
	global_store_dwordx4 v[6:7], v[28:31], off offset:1024 nt
	global_store_dwordx4 v[6:7], v[32:35], off offset:2048 nt
	global_store_dwordx4 v[6:7], v[36:39], off offset:3072 nt
	v_lshl_add_u64 v[6:7], v[6:7], 0, s[4:5]
	s_cbranch_scc1 .LBB0_1445
